# stack10 body shifted by 64 B, second measurement (choosing between two placements of the same code)
# speedup vs baseline: 1.0071x; 1.0034x over previous
; #define LAS __attribute__((address_space(3)))
; __global__ void __launch_bounds__(NWAVES * 64, 2) fwd(Args args) {
;     extern __shared__ __attribute__((aligned(16))) unsigned char lds_raw[];
;     LAS unsigned char* lds = (LAS unsigned char*)lds_raw;
;     ...
;     const int tid0 = threadIdx.x, wave = __builtin_amdgcn_readfirstlane(tid0 >> 6);
;     const int G = gridDim.x; const int bx = blockIdx.x; const int vcu = (G % 8 == 0) ? (bx % 8) * (G / 8) + bx / 8 : bx;
;     unsigned char* ws = args.ws;
;     gu32* ctl = (gu32*)(ws + WS_CTL);
;     for (int u = tid0; u < (LDS_BYTES - LDSCTL_OFF) / 4; u += NWAVES * 64) ((LAS unsigned*)(lds + LDSCTL_OFF))[u] = 0u;
.LBB0_2:
	s_load_dwordx16 s[8:23], s[0:1], 0x0
	v_lshl_add_u32 v0, v234, 2, 0
	v_add_u32_e32 v0, 0x21800, v0
	s_mov_b32 s5, 1
	v_mov_b32_e32 v1, 0
	s_waitcnt lgkmcnt(0)
	v_writelane_b32 v250, s8, 2
	s_mov_b32 s6, s4
	s_nop 0
	v_writelane_b32 v250, s9, 3
	v_writelane_b32 v250, s10, 4
	v_writelane_b32 v250, s11, 5
	v_writelane_b32 v250, s12, 6
	v_writelane_b32 v250, s13, 7
	v_writelane_b32 v250, s14, 8
	v_writelane_b32 v250, s15, 9
	v_writelane_b32 v250, s16, 10
	v_writelane_b32 v250, s17, 11
	v_writelane_b32 v250, s18, 12
	v_writelane_b32 v250, s19, 13
	v_writelane_b32 v250, s20, 14
	v_writelane_b32 v250, s21, 15
	v_writelane_b32 v250, s22, 16
	v_writelane_b32 v250, s23, 17
	s_load_dwordx16 s[16:31], s[0:1], 0x40
	s_mov_b64 s[0:1], 0
	s_branch .LBB0_4
	s_nop 0
	s_nop 0
	s_nop 0
	s_nop 0
	s_nop 0
	s_nop 0
	s_nop 0
	s_nop 0
	s_nop 0
	s_nop 0
	s_nop 0
	s_nop 0
	s_nop 0
	s_nop 0
	s_nop 0
	s_nop 0
